# plus gemm_qkv workgroup-id bit swap: first dispatch round mixes q/k and v tiles so epilogue HBM bursts overlap other tiles' main loops
# speedup vs baseline: 1.0168x; 1.0040x over previous
_Z8gemm_qkvPKDF16_S0_7EpiArgs:
	s_load_dwordx4 s[4:7], s[0:1], 0x0
	s_lshr_b32 s3, s2, 1
	s_xor_b32 s3, s3, s2
	s_and_b32 s3, s3, 0x80
	s_xor_b32 s2, s2, s3
	s_lshl_b32 s3, s3, 1
	s_xor_b32 s2, s2, s3
	s_cmpk_gt_u32 s2, 0xff
	s_waitcnt lgkmcnt(0)
	s_mov_b64 s[8:9], s[6:7]
	s_mov_b64 s[6:7], -1
	s_cbranch_scc1 .LBB2_3
	s_and_b64 vcc, exec, s[6:7]
	s_cbranch_vccnz .LBB2_16
